# NA unit now interleaves PV and QK MFMAs into the softmax VALU stream with double-buffered scores
# speedup vs baseline: 1.0026x; 1.0026x over previous
; #define LAS __attribute__((address_space(3)))
; template <bool WIN>
; __device__ __forceinline__ void na_unit(Frame& F, int b, int h, int r, int strip) {
;     ...
;     int ln_ = F.lane; asm volatile("" : "+v"(ln_));
;     const int i = ln_ & 15, g = ln_ >> 4;
;     const int qrow0 = WIN ? (b * SEQ + r * 64 + strip * 16) : (NLAT + b * CTXL + strip * 16);
;     const int ki = 8 * (i >> 2) + (i & 3);
;     const unsigned qlo = (unsigned)((i * DIN + 8 * g) * 2), klo = (unsigned)((ki * DIN + 8 * g) * 2), vlo = (unsigned)((i * SPB + 8 * g) * 2);
;     const char* qb = uni_ptr((const char*)(U + (size_t)qrow0 * DIN + UQ + h * 64));
;     const bf16x8 q0 = gld16o(qb, qlo), q1 = gld16o(qb + 64, qlo);
;     int kr0 = 0, u0 = 0;
;     if (WIN) { kr0 = r - 4; kr0 = kr0 < 0 ? 0 : (kr0 > 56 ? 56 : kr0); u0 = strip == 0 ? 0 : (strip == 1 ? 8 : (strip == 2 ? 24 : 32)); }
;     const LAS bf16_t* KR = (const LAS bf16_t*)(F.lds + NA_KR);
;     const char* vbase = uni_ptr((const char*)(VT + kr0 * 64 + u0));
;     f32x4 o[4];
; #pragma unroll
;     for (int d = 0; d < 4; ++d) o[d] = (f32x4){0.f, 0.f, 0.f, 0.f};
;     float lsum = 0.f;
;     ...
;     bf16x8 vA[4], vB[4], vC[4];
;     if (WIN) { NA_WLOAD(vA, 0); NA_WLOAD(vB, 1); NA_WLOAD(vC, 2); NA_SB(); }
; #pragma unroll
;     for (int cc = 0; cc < 8; ++cc) {
;         bf16x8 kc[2][2], vc[4]; f32x4 sc[2];
; #pragma unroll
;         for (int t = 0; t < 2; ++t) { const LAS bf16_t* kp = KC + (cc * 32 + ki + 4 * t) * 72 + 8 * g; kc[t][0] = *(const LAS bf16x8*)kp; kc[t][1] = *(const LAS bf16x8*)(kp + 32); }
; #pragma unroll
;         for (int d = 0; d < 4; ++d) vc[d] = *(const LAS bf16x8*)(VC + (d * 16 + i) * 264 + cc * 32 + 8 * g);
;         NA_QK(kc, sc);
; #pragma unroll
;         for (int t = 0; t < 2; ++t)
; #pragma unroll
;             for (int e = 0; e < 4; ++e) { const float p = __builtin_amdgcn_exp2f(fminf(sc[t][e], NA_CLAMP)); sc[t][e] = p; lsum += p; }
;         NA_PV(sc, vc);
;     }
;     if (WIN) {
;         const int c = strip * 16 + i; int kc0 = c - 8; kc0 = kc0 < 0 ? 0 : (kc0 > 48 ? 48 : kc0);
;         int dcl[2][4]; bool okm[2][4];
; #pragma unroll
;         for (int t = 0; t < 2; ++t)
; #pragma unroll
;             for (int e = 0; e < 4; ++e) { const int kc = u0 + 8 * g + 4 * t + e; okm[t][e] = (kc >= kc0) && (kc < kc0 + 16); int dc = kc - c + 15; dcl[t][e] = okm[t][e] ? (dc < 0 ? 0 : (dc > 30 ? 30 : dc)) : 31; }
.Lna_nostag:
	s_sub_i32 s3, s76, 4
	s_max_i32 s3, s3, 0
	s_min_i32 s3, s3, 56
	s_mov_b32 s18, 0x42ad1f97
	s_mov_b32 s20, s79
	s_mov_b32 s21, s80
	v_lshrrev_b32_e32 v225, 2, v98
	v_and_b32_e32 v236, 3, v98
	v_lshl_or_b32 v225, v225, 3, v236
	v_lshlrev_b32_e32 v237, 1, v99
	s_movk_i32 s4, 0x90
	s_movk_i32 s5, 0x210
	s_movk_i32 s8, 0x2200
	v_mad_u32_u24 v200, v225, s4, v237
	v_add_u32_e32 v200, 0x800, v200
	v_mad_u32_u24 v201, v98, s5, v237
	v_add_u32_e32 v201, 0x9800, v201
	ds_read_b128 v[44:47], v200 offset:0
	ds_read_b128 v[48:51], v200 offset:64
	ds_read_b128 v[52:55], v200 offset:576
	ds_read_b128 v[56:59], v200 offset:640
	ds_read_b128 v[60:63], v201 offset:0
	ds_read_b128 v[64:67], v201 offset:8448
	ds_read_b128 v[68:71], v201 offset:16896
	ds_read_b128 v[72:75], v201 offset:25344
	s_lshl_b32 s0, s3, 6
	s_add_i32 s0, s0, s2
	s_lshl_b32 s0, s0, 1
	v_mad_u32_u24 v204, v98, s8, v237
	v_add_u32_e32 v204, s0, v204
	v_add_u32_e32 v205, 0x22000, v204
	v_add_u32_e32 v206, 0x44000, v204
	v_add_u32_e32 v207, 0x66000, v204
	global_load_dwordx4 v[104:107], v204, s[20:21] offset:0
	global_load_dwordx4 v[108:111], v205, s[20:21] offset:0
	global_load_dwordx4 v[112:115], v206, s[20:21] offset:0
	global_load_dwordx4 v[116:119], v207, s[20:21] offset:0
	global_load_dwordx4 v[120:123], v204, s[20:21] offset:128
	global_load_dwordx4 v[124:127], v205, s[20:21] offset:128
	global_load_dwordx4 v[128:131], v206, s[20:21] offset:128
	global_load_dwordx4 v[132:135], v207, s[20:21] offset:128
	global_load_dwordx4 v[156:159], v204, s[20:21] offset:256
	global_load_dwordx4 v[160:163], v205, s[20:21] offset:256
	global_load_dwordx4 v[164:167], v206, s[20:21] offset:256
	global_load_dwordx4 v[168:171], v207, s[20:21] offset:256
	global_load_dwordx4 v[172:175], v204, s[20:21] offset:384
	global_load_dwordx4 v[176:179], v205, s[20:21] offset:384
	global_load_dwordx4 v[180:183], v206, s[20:21] offset:384
	global_load_dwordx4 v[184:187], v207, s[20:21] offset:384
	s_mul_i32 s0, s2, 0x90
	s_add_i32 s0, s0, 0x11400
	v_add_u32_e32 v202, s0, v200
	s_sub_i32 s9, s3, s76
	s_add_i32 s9, s9, 7
	s_lshl_b32 s9, s9, 7
	s_lshl_b32 s0, s59, 4
	v_add_u32_e32 v238, s0, v98
	v_add_u32_e32 v239, -8, v238
	v_med3_i32 v239, v239, 0, 48
	v_add_u32_e32 v240, s2, v99
	v_mov_b32_e32 v244, 31
	v_add_u32_e32 v241, 0, v240
	v_sub_u32_e32 v242, v241, v239
	v_sub_u32_e32 v243, v241, v238
	v_cmp_gt_u32_e32 vcc, 16, v242
	v_add_u32_e32 v243, 15, v243
	v_med3_i32 v243, v243, 0, 30
	v_cndmask_b32_e32 v243, v244, v243, vcc
	v_lshl_add_u32 v216, v243, 2, s9
	v_add_u32_e32 v241, 1, v240
	v_sub_u32_e32 v242, v241, v239
	v_sub_u32_e32 v243, v241, v238
	v_cmp_gt_u32_e32 vcc, 16, v242
	v_add_u32_e32 v243, 15, v243
	v_med3_i32 v243, v243, 0, 30
	v_cndmask_b32_e32 v243, v244, v243, vcc
	v_lshl_add_u32 v217, v243, 2, s9
	v_add_u32_e32 v241, 2, v240
	v_sub_u32_e32 v242, v241, v239
	v_sub_u32_e32 v243, v241, v238
	v_cmp_gt_u32_e32 vcc, 16, v242
	v_add_u32_e32 v243, 15, v243
	v_med3_i32 v243, v243, 0, 30
	v_cndmask_b32_e32 v243, v244, v243, vcc
	v_lshl_add_u32 v218, v243, 2, s9
	v_add_u32_e32 v241, 3, v240
	v_sub_u32_e32 v242, v241, v239
	v_sub_u32_e32 v243, v241, v238
	v_cmp_gt_u32_e32 vcc, 16, v242
	v_add_u32_e32 v243, 15, v243
	v_med3_i32 v243, v243, 0, 30
	v_cndmask_b32_e32 v243, v244, v243, vcc
	v_lshl_add_u32 v219, v243, 2, s9
	v_add_u32_e32 v241, 4, v240
	v_sub_u32_e32 v242, v241, v239
	v_sub_u32_e32 v243, v241, v238
	v_cmp_gt_u32_e32 vcc, 16, v242
	v_add_u32_e32 v243, 15, v243
	v_med3_i32 v243, v243, 0, 30
	v_cndmask_b32_e32 v243, v244, v243, vcc
	v_lshl_add_u32 v220, v243, 2, s9
	v_add_u32_e32 v241, 5, v240
	v_sub_u32_e32 v242, v241, v239
	v_sub_u32_e32 v243, v241, v238
	v_cmp_gt_u32_e32 vcc, 16, v242
	v_add_u32_e32 v243, 15, v243
	v_med3_i32 v243, v243, 0, 30
	v_cndmask_b32_e32 v243, v244, v243, vcc
	v_lshl_add_u32 v221, v243, 2, s9
	v_add_u32_e32 v241, 6, v240
	v_sub_u32_e32 v242, v241, v239
	v_sub_u32_e32 v243, v241, v238
	v_cmp_gt_u32_e32 vcc, 16, v242
	v_add_u32_e32 v243, 15, v243
	v_med3_i32 v243, v243, 0, 30
	v_cndmask_b32_e32 v243, v244, v243, vcc
	v_lshl_add_u32 v222, v243, 2, s9
	v_add_u32_e32 v241, 7, v240
	v_sub_u32_e32 v242, v241, v239
	v_sub_u32_e32 v243, v241, v238
	v_cmp_gt_u32_e32 vcc, 16, v242
	v_add_u32_e32 v243, 15, v243
	v_med3_i32 v243, v243, 0, 30
	v_cndmask_b32_e32 v243, v244, v243, vcc
	v_lshl_add_u32 v223, v243, 2, s9
	v_lshl_add_u32 v224, v98, 11, v99
	s_lshl_b32 s0, s48, 11
	s_add_u32 s10, s81, s0
	s_addc_u32 s11, s82, 0
	v_lshlrev_b32_e32 v246, 2, v100
	v_xor_b32_e32 v247, 0x80, v246
	v_xor_b32_e32 v246, 64, v246
	v_mov_b32_e32 v16, 0
	v_mov_b32_e32 v17, 0
	v_mov_b32_e32 v18, 0
	v_mov_b32_e32 v19, 0
	v_mov_b32_e32 v20, 0
	v_mov_b32_e32 v21, 0
	v_mov_b32_e32 v22, 0
	v_mov_b32_e32 v23, 0
	v_mov_b32_e32 v24, 0
	v_mov_b32_e32 v25, 0
	v_mov_b32_e32 v26, 0
	v_mov_b32_e32 v27, 0
	v_mov_b32_e32 v28, 0
	v_mov_b32_e32 v29, 0
	v_mov_b32_e32 v30, 0
	v_mov_b32_e32 v31, 0
	v_mov_b32_e32 v198, 0
	v_mov_b32_e32 v199, 0
	s_mul_i32 s0, s3, 57
	s_bfe_u32 s0, s0, 0x70009
	s_mul_i32 s0, s0, 9
	s_sub_i32 s19, s3, s0
	s_waitcnt vmcnt(16) lgkmcnt(4)
	v_mfma_f32_16x16x32_bf16 v[32:35], v[44:47], v[12:15], 0
	v_mfma_f32_16x16x32_bf16 v[36:39], v[52:55], v[12:15], 0
	v_mfma_f32_16x16x32_bf16 v[32:35], v[48:51], v[8:11], v[32:35]
	v_mfma_f32_16x16x32_bf16 v[36:39], v[56:59], v[8:11], v[36:39]
	ds_read_b128 v[44:47], v200 offset:4608
	ds_read_b128 v[48:51], v200 offset:4672
	ds_read_b128 v[52:55], v200 offset:5184
	ds_read_b128 v[56:59], v200 offset:5248
	s_nop 2
	v_min_f32_e32 v32, s18, v32
	v_min_f32_e32 v33, s18, v33
	v_min_f32_e32 v34, s18, v34
	s_waitcnt lgkmcnt(0)
; #define LAS __attribute__((address_space(3)))
; #define NA_QK(kb_, s_) do { _Pragma("unroll") for (int t = 0; t < 2; ++t) { f32x4 a = (f32x4){0.f, 0.f, 0.f, 0.f}; a = mfma16(kb_[t][0], q0, a); a = mfma16(kb_[t][1], q1, a); s_[t] = a; } } while (0)
; #define NA_PV(s_, vb_) do { u32x4 pw; pw.x = pk2(s_[0][0], s_[0][1]); pw.y = pk2(s_[0][2], s_[0][3]); pw.z = pk2(s_[1][0], s_[1][1]); pw.w = pk2(s_[1][2], s_[1][3]); const bf16x8 pf = __builtin_bit_cast(bf16x8, pw); \
;         _Pragma("unroll") for (int d = 0; d < 4; ++d) o[d] = mfma16(vb_[d], pf, o[d]); } while (0)
; template <bool WIN>
; __device__ __forceinline__ void na_unit(Frame& F, int b, int h, int r, int strip) {
;     ...
; #pragma unroll
;     for (int cc = 0; cc < 8; ++cc) {
;         bf16x8 kc[2][2], vc[4]; f32x4 sc[2];
; #pragma unroll
;         for (int t = 0; t < 2; ++t) { const LAS bf16_t* kp = KC + (cc * 32 + ki + 4 * t) * 72 + 8 * g; kc[t][0] = *(const LAS bf16x8*)kp; kc[t][1] = *(const LAS bf16x8*)(kp + 32); }
; #pragma unroll
;         for (int d = 0; d < 4; ++d) vc[d] = *(const LAS bf16x8*)(VC + (d * 16 + i) * 264 + cc * 32 + 8 * g);
;         NA_QK(kc, sc);
; #pragma unroll
;         for (int t = 0; t < 2; ++t)
; #pragma unroll
;             for (int e = 0; e < 4; ++e) { const float p = __builtin_amdgcn_exp2f(fminf(sc[t][e], NA_CLAMP)); sc[t][e] = p; lsum += p; }
;         NA_PV(sc, vc);
;     }
	v_mfma_f32_16x16x32_bf16 v[84:87], v[44:47], v[12:15], 0
	v_min_f32_e32 v35, s18, v35
	v_min_f32_e32 v36, s18, v36
	v_min_f32_e32 v37, s18, v37
	v_mfma_f32_16x16x32_bf16 v[90:93], v[52:55], v[12:15], 0
	v_min_f32_e32 v38, s18, v38
	v_min_f32_e32 v39, s18, v39
	v_exp_f32_e32 v32, v32
	v_mfma_f32_16x16x32_bf16 v[84:87], v[48:51], v[8:11], v[84:87]
	v_exp_f32_e32 v33, v33
	v_exp_f32_e32 v34, v34
	v_exp_f32_e32 v35, v35
	v_mfma_f32_16x16x32_bf16 v[90:93], v[56:59], v[8:11], v[90:93]
	v_exp_f32_e32 v36, v36
	v_exp_f32_e32 v37, v37
	v_exp_f32_e32 v38, v38
	v_exp_f32_e32 v39, v39
	v_add_f32_e32 v198, v198, v32
	v_add_f32_e32 v199, v199, v36
	v_add_f32_e32 v198, v198, v33
	v_add_f32_e32 v199, v199, v37
	v_add_f32_e32 v198, v198, v34
	v_add_f32_e32 v199, v199, v38
	v_add_f32_e32 v198, v198, v35
	v_add_f32_e32 v199, v199, v39
	v_cvt_pk_bf16_f32 v40, v32, v33
	v_cvt_pk_bf16_f32 v41, v34, v35
	v_cvt_pk_bf16_f32 v42, v36, v37
	v_cvt_pk_bf16_f32 v43, v38, v39
	ds_read_b128 v[44:47], v200 offset:9216
	ds_read_b128 v[48:51], v200 offset:9280
	ds_read_b128 v[52:55], v200 offset:9792
	ds_read_b128 v[56:59], v200 offset:9856
	v_min_f32_e32 v84, s18, v84
	v_min_f32_e32 v85, s18, v85
	v_min_f32_e32 v86, s18, v86
	v_mfma_f32_16x16x32_bf16 v[16:19], v[60:63], v[40:43], v[16:19]
	v_min_f32_e32 v87, s18, v87
	v_min_f32_e32 v90, s18, v90
	v_min_f32_e32 v91, s18, v91
	v_mfma_f32_16x16x32_bf16 v[20:23], v[64:67], v[40:43], v[20:23]
	v_min_f32_e32 v92, s18, v92
	v_min_f32_e32 v93, s18, v93
	v_exp_f32_e32 v84, v84
	v_mfma_f32_16x16x32_bf16 v[24:27], v[68:71], v[40:43], v[24:27]
	v_exp_f32_e32 v85, v85
	v_exp_f32_e32 v86, v86
	v_exp_f32_e32 v87, v87
	v_mfma_f32_16x16x32_bf16 v[28:31], v[72:75], v[40:43], v[28:31]
	ds_read_b128 v[60:63], v201 offset:64
	ds_read_b128 v[64:67], v201 offset:8512
	ds_read_b128 v[68:71], v201 offset:16960
	ds_read_b128 v[72:75], v201 offset:25408
	v_exp_f32_e32 v90, v90
	v_exp_f32_e32 v91, v91
	v_exp_f32_e32 v92, v92
	s_waitcnt lgkmcnt(4)
	v_mfma_f32_16x16x32_bf16 v[32:35], v[44:47], v[12:15], 0
	v_exp_f32_e32 v93, v93
	v_add_f32_e32 v198, v198, v84
	v_add_f32_e32 v199, v199, v90
	v_mfma_f32_16x16x32_bf16 v[36:39], v[52:55], v[12:15], 0
	v_add_f32_e32 v198, v198, v85
	v_add_f32_e32 v199, v199, v91
	v_add_f32_e32 v198, v198, v86
	v_mfma_f32_16x16x32_bf16 v[32:35], v[48:51], v[8:11], v[32:35]
	v_add_f32_e32 v199, v199, v92
	v_add_f32_e32 v198, v198, v87
	v_add_f32_e32 v199, v199, v93
	v_mfma_f32_16x16x32_bf16 v[36:39], v[56:59], v[8:11], v[36:39]
	v_cvt_pk_bf16_f32 v142, v84, v85
	v_cvt_pk_bf16_f32 v143, v86, v87
	v_cvt_pk_bf16_f32 v144, v90, v91
	v_cvt_pk_bf16_f32 v145, v92, v93
	ds_read_b128 v[44:47], v200 offset:13824
	ds_read_b128 v[48:51], v200 offset:13888
	ds_read_b128 v[52:55], v200 offset:14400
	ds_read_b128 v[56:59], v200 offset:14464
	v_min_f32_e32 v32, s18, v32
	v_min_f32_e32 v33, s18, v33
	v_min_f32_e32 v34, s18, v34
	s_waitcnt lgkmcnt(4)
	v_mfma_f32_16x16x32_bf16 v[16:19], v[60:63], v[142:145], v[16:19]
	v_min_f32_e32 v35, s18, v35
	v_min_f32_e32 v36, s18, v36
	v_min_f32_e32 v37, s18, v37
	v_mfma_f32_16x16x32_bf16 v[20:23], v[64:67], v[142:145], v[20:23]
	v_min_f32_e32 v38, s18, v38
	v_min_f32_e32 v39, s18, v39
	v_exp_f32_e32 v32, v32
	v_mfma_f32_16x16x32_bf16 v[24:27], v[68:71], v[142:145], v[24:27]
	v_exp_f32_e32 v33, v33
	v_exp_f32_e32 v34, v34
	v_exp_f32_e32 v35, v35
	v_mfma_f32_16x16x32_bf16 v[28:31], v[72:75], v[142:145], v[28:31]
	ds_read_b128 v[60:63], v201 offset:128
	ds_read_b128 v[64:67], v201 offset:8576
	ds_read_b128 v[68:71], v201 offset:17024
	ds_read_b128 v[72:75], v201 offset:25472
	v_exp_f32_e32 v36, v36
	v_exp_f32_e32 v37, v37
	v_exp_f32_e32 v38, v38
	s_waitcnt lgkmcnt(4)
	v_mfma_f32_16x16x32_bf16 v[84:87], v[44:47], v[12:15], 0
	v_exp_f32_e32 v39, v39
	v_add_f32_e32 v198, v198, v32
	v_add_f32_e32 v199, v199, v36
	v_mfma_f32_16x16x32_bf16 v[90:93], v[52:55], v[12:15], 0
	v_add_f32_e32 v198, v198, v33
	v_add_f32_e32 v199, v199, v37
	v_add_f32_e32 v198, v198, v34
	v_mfma_f32_16x16x32_bf16 v[84:87], v[48:51], v[8:11], v[84:87]
	v_add_f32_e32 v199, v199, v38
	v_add_f32_e32 v198, v198, v35
	v_add_f32_e32 v199, v199, v39
	v_mfma_f32_16x16x32_bf16 v[90:93], v[56:59], v[8:11], v[90:93]
	v_cvt_pk_bf16_f32 v40, v32, v33
	v_cvt_pk_bf16_f32 v41, v34, v35
	v_cvt_pk_bf16_f32 v42, v36, v37
	v_cvt_pk_bf16_f32 v43, v38, v39
	ds_read_b128 v[44:47], v200 offset:18432
	ds_read_b128 v[48:51], v200 offset:18496
	ds_read_b128 v[52:55], v200 offset:19008
	ds_read_b128 v[56:59], v200 offset:19072
	v_min_f32_e32 v84, s18, v84
	v_min_f32_e32 v85, s18, v85
	v_min_f32_e32 v86, s18, v86
	s_waitcnt lgkmcnt(4)
	v_mfma_f32_16x16x32_bf16 v[16:19], v[60:63], v[40:43], v[16:19]
	v_min_f32_e32 v87, s18, v87
	v_min_f32_e32 v90, s18, v90
	v_min_f32_e32 v91, s18, v91
	v_mfma_f32_16x16x32_bf16 v[20:23], v[64:67], v[40:43], v[20:23]
	v_min_f32_e32 v92, s18, v92
	v_min_f32_e32 v93, s18, v93
	v_exp_f32_e32 v84, v84
	v_mfma_f32_16x16x32_bf16 v[24:27], v[68:71], v[40:43], v[24:27]
	v_exp_f32_e32 v85, v85
	v_exp_f32_e32 v86, v86
	v_exp_f32_e32 v87, v87
	v_mfma_f32_16x16x32_bf16 v[28:31], v[72:75], v[40:43], v[28:31]
	ds_read_b128 v[60:63], v201 offset:192
	ds_read_b128 v[64:67], v201 offset:8640
	ds_read_b128 v[68:71], v201 offset:17088
	ds_read_b128 v[72:75], v201 offset:25536
	v_exp_f32_e32 v90, v90
	v_exp_f32_e32 v91, v91
	v_exp_f32_e32 v92, v92
	s_waitcnt lgkmcnt(4)
; #define LAS __attribute__((address_space(3)))
; #define NA_QK(kb_, s_) do { _Pragma("unroll") for (int t = 0; t < 2; ++t) { f32x4 a = (f32x4){0.f, 0.f, 0.f, 0.f}; a = mfma16(kb_[t][0], q0, a); a = mfma16(kb_[t][1], q1, a); s_[t] = a; } } while (0)
; #define NA_PV(s_, vb_) do { u32x4 pw; pw.x = pk2(s_[0][0], s_[0][1]); pw.y = pk2(s_[0][2], s_[0][3]); pw.z = pk2(s_[1][0], s_[1][1]); pw.w = pk2(s_[1][2], s_[1][3]); const bf16x8 pf = __builtin_bit_cast(bf16x8, pw); \
;         _Pragma("unroll") for (int d = 0; d < 4; ++d) o[d] = mfma16(vb_[d], pf, o[d]); } while (0)
; template <bool WIN>
; __device__ __forceinline__ void na_unit(Frame& F, int b, int h, int r, int strip) {
;     ...
; #pragma unroll
;     for (int cc = 0; cc < 8; ++cc) {
;         bf16x8 kc[2][2], vc[4]; f32x4 sc[2];
; #pragma unroll
;         for (int t = 0; t < 2; ++t) { const LAS bf16_t* kp = KC + (cc * 32 + ki + 4 * t) * 72 + 8 * g; kc[t][0] = *(const LAS bf16x8*)kp; kc[t][1] = *(const LAS bf16x8*)(kp + 32); }
; #pragma unroll
;         for (int d = 0; d < 4; ++d) vc[d] = *(const LAS bf16x8*)(VC + (d * 16 + i) * 264 + cc * 32 + 8 * g);
;         NA_QK(kc, sc);
; #pragma unroll
;         for (int t = 0; t < 2; ++t)
; #pragma unroll
;             for (int e = 0; e < 4; ++e) { const float p = __builtin_amdgcn_exp2f(fminf(sc[t][e], NA_CLAMP)); sc[t][e] = p; lsum += p; }
;         NA_PV(sc, vc);
;     }
	v_mfma_f32_16x16x32_bf16 v[32:35], v[44:47], v[12:15], 0
	v_exp_f32_e32 v93, v93
	v_add_f32_e32 v198, v198, v84
	v_add_f32_e32 v199, v199, v90
	v_mfma_f32_16x16x32_bf16 v[36:39], v[52:55], v[12:15], 0
	v_add_f32_e32 v198, v198, v85
	v_add_f32_e32 v199, v199, v91
	v_add_f32_e32 v198, v198, v86
	v_mfma_f32_16x16x32_bf16 v[32:35], v[48:51], v[8:11], v[32:35]
	v_add_f32_e32 v199, v199, v92
	v_add_f32_e32 v198, v198, v87
	v_add_f32_e32 v199, v199, v93
	v_mfma_f32_16x16x32_bf16 v[36:39], v[56:59], v[8:11], v[36:39]
	v_cvt_pk_bf16_f32 v142, v84, v85
	v_cvt_pk_bf16_f32 v143, v86, v87
	v_cvt_pk_bf16_f32 v144, v90, v91
	v_cvt_pk_bf16_f32 v145, v92, v93
	ds_read_b128 v[44:47], v200 offset:23040
	ds_read_b128 v[48:51], v200 offset:23104
	ds_read_b128 v[52:55], v200 offset:23616
	ds_read_b128 v[56:59], v200 offset:23680
	v_min_f32_e32 v32, s18, v32
	v_min_f32_e32 v33, s18, v33
	v_min_f32_e32 v34, s18, v34
	s_waitcnt lgkmcnt(4)
	v_mfma_f32_16x16x32_bf16 v[16:19], v[60:63], v[142:145], v[16:19]
	v_min_f32_e32 v35, s18, v35
	v_min_f32_e32 v36, s18, v36
	v_min_f32_e32 v37, s18, v37
	v_mfma_f32_16x16x32_bf16 v[20:23], v[64:67], v[142:145], v[20:23]
	v_min_f32_e32 v38, s18, v38
	v_min_f32_e32 v39, s18, v39
	v_exp_f32_e32 v32, v32
	v_mfma_f32_16x16x32_bf16 v[24:27], v[68:71], v[142:145], v[24:27]
	v_exp_f32_e32 v33, v33
	v_exp_f32_e32 v34, v34
	v_exp_f32_e32 v35, v35
	v_mfma_f32_16x16x32_bf16 v[28:31], v[72:75], v[142:145], v[28:31]
	ds_read_b128 v[60:63], v201 offset:256
	ds_read_b128 v[64:67], v201 offset:8704
	ds_read_b128 v[68:71], v201 offset:17152
	ds_read_b128 v[72:75], v201 offset:25600
	v_exp_f32_e32 v36, v36
	v_exp_f32_e32 v37, v37
	v_exp_f32_e32 v38, v38
	s_waitcnt lgkmcnt(4)
	v_mfma_f32_16x16x32_bf16 v[84:87], v[44:47], v[12:15], 0
	v_exp_f32_e32 v39, v39
	v_add_f32_e32 v198, v198, v32
	v_add_f32_e32 v199, v199, v36
	v_mfma_f32_16x16x32_bf16 v[90:93], v[52:55], v[12:15], 0
	v_add_f32_e32 v198, v198, v33
	v_add_f32_e32 v199, v199, v37
	v_add_f32_e32 v198, v198, v34
	v_mfma_f32_16x16x32_bf16 v[84:87], v[48:51], v[8:11], v[84:87]
	v_add_f32_e32 v199, v199, v38
	v_add_f32_e32 v198, v198, v35
	v_add_f32_e32 v199, v199, v39
	v_mfma_f32_16x16x32_bf16 v[90:93], v[56:59], v[8:11], v[90:93]
	v_cvt_pk_bf16_f32 v40, v32, v33
	v_cvt_pk_bf16_f32 v41, v34, v35
	v_cvt_pk_bf16_f32 v42, v36, v37
	v_cvt_pk_bf16_f32 v43, v38, v39
	ds_read_b128 v[44:47], v200 offset:27648
	ds_read_b128 v[48:51], v200 offset:27712
	ds_read_b128 v[52:55], v200 offset:28224
	ds_read_b128 v[56:59], v200 offset:28288
	v_min_f32_e32 v84, s18, v84
	v_min_f32_e32 v85, s18, v85
	v_min_f32_e32 v86, s18, v86
	s_waitcnt lgkmcnt(4)
	v_mfma_f32_16x16x32_bf16 v[16:19], v[60:63], v[40:43], v[16:19]
	v_min_f32_e32 v87, s18, v87
	v_min_f32_e32 v90, s18, v90
	v_min_f32_e32 v91, s18, v91
	v_mfma_f32_16x16x32_bf16 v[20:23], v[64:67], v[40:43], v[20:23]
	v_min_f32_e32 v92, s18, v92
	v_min_f32_e32 v93, s18, v93
	v_exp_f32_e32 v84, v84
	v_mfma_f32_16x16x32_bf16 v[24:27], v[68:71], v[40:43], v[24:27]
	v_exp_f32_e32 v85, v85
	v_exp_f32_e32 v86, v86
	v_exp_f32_e32 v87, v87
	v_mfma_f32_16x16x32_bf16 v[28:31], v[72:75], v[40:43], v[28:31]
	ds_read_b128 v[60:63], v201 offset:320
	ds_read_b128 v[64:67], v201 offset:8768
	ds_read_b128 v[68:71], v201 offset:17216
	ds_read_b128 v[72:75], v201 offset:25664
	v_exp_f32_e32 v90, v90
	v_exp_f32_e32 v91, v91
	v_exp_f32_e32 v92, v92
	s_waitcnt lgkmcnt(4)
	v_mfma_f32_16x16x32_bf16 v[32:35], v[44:47], v[12:15], 0
	v_exp_f32_e32 v93, v93
	v_add_f32_e32 v198, v198, v84
	v_add_f32_e32 v199, v199, v90
	v_mfma_f32_16x16x32_bf16 v[36:39], v[52:55], v[12:15], 0
	v_add_f32_e32 v198, v198, v85
	v_add_f32_e32 v199, v199, v91
	v_add_f32_e32 v198, v198, v86
	v_mfma_f32_16x16x32_bf16 v[32:35], v[48:51], v[8:11], v[32:35]
	v_add_f32_e32 v199, v199, v92
	v_add_f32_e32 v198, v198, v87
	v_add_f32_e32 v199, v199, v93
	v_mfma_f32_16x16x32_bf16 v[36:39], v[56:59], v[8:11], v[36:39]
	v_cvt_pk_bf16_f32 v142, v84, v85
	v_cvt_pk_bf16_f32 v143, v86, v87
	v_cvt_pk_bf16_f32 v144, v90, v91
	v_cvt_pk_bf16_f32 v145, v92, v93
	ds_read_b128 v[44:47], v200 offset:32256
	ds_read_b128 v[48:51], v200 offset:32320
	ds_read_b128 v[52:55], v200 offset:32832
	ds_read_b128 v[56:59], v200 offset:32896
	v_min_f32_e32 v32, s18, v32
	v_min_f32_e32 v33, s18, v33
	v_min_f32_e32 v34, s18, v34
	s_waitcnt lgkmcnt(4)
	v_mfma_f32_16x16x32_bf16 v[16:19], v[60:63], v[142:145], v[16:19]
	v_min_f32_e32 v35, s18, v35
	v_min_f32_e32 v36, s18, v36
	v_min_f32_e32 v37, s18, v37
	v_mfma_f32_16x16x32_bf16 v[20:23], v[64:67], v[142:145], v[20:23]
	v_min_f32_e32 v38, s18, v38
	v_min_f32_e32 v39, s18, v39
	v_exp_f32_e32 v32, v32
	v_mfma_f32_16x16x32_bf16 v[24:27], v[68:71], v[142:145], v[24:27]
	v_exp_f32_e32 v33, v33
	v_exp_f32_e32 v34, v34
	v_exp_f32_e32 v35, v35
	v_mfma_f32_16x16x32_bf16 v[28:31], v[72:75], v[142:145], v[28:31]
	ds_read_b128 v[60:63], v201 offset:384
	ds_read_b128 v[64:67], v201 offset:8832
	ds_read_b128 v[68:71], v201 offset:17280
	ds_read_b128 v[72:75], v201 offset:25728
	v_exp_f32_e32 v36, v36
	v_exp_f32_e32 v37, v37
	v_exp_f32_e32 v38, v38
	s_waitcnt lgkmcnt(4)
; #define LAS __attribute__((address_space(3)))
; #define NA_SB() __builtin_amdgcn_sched_barrier(0)
; #define NA_WLOAD(vb_, cw) do { _Pragma("unroll") for (int d = 0; d < 4; ++d) vb_[d] = gld16o(vbase + ((size_t)(d * 16) * SPB + (cw) * 64) * 2, vlo); } while (0)
; #define NA_QK(kb_, s_) do { _Pragma("unroll") for (int t = 0; t < 2; ++t) { f32x4 a = (f32x4){0.f, 0.f, 0.f, 0.f}; a = mfma16(kb_[t][0], q0, a); a = mfma16(kb_[t][1], q1, a); s_[t] = a; } } while (0)
; #define NA_PV(s_, vb_) do { u32x4 pw; pw.x = pk2(s_[0][0], s_[0][1]); pw.y = pk2(s_[0][2], s_[0][3]); pw.z = pk2(s_[1][0], s_[1][1]); pw.w = pk2(s_[1][2], s_[1][3]); const bf16x8 pf = __builtin_bit_cast(bf16x8, pw); \
;         _Pragma("unroll") for (int d = 0; d < 4; ++d) o[d] = mfma16(vb_[d], pf, o[d]); } while (0)
; template <bool WIN>
; __device__ __forceinline__ void na_unit(Frame& F, int b, int h, int r, int strip) {
;     ...
; #pragma unroll
;     for (int cc = 0; cc < 8; ++cc) {
;         bf16x8 kc[2][2], vc[4]; f32x4 sc[2];
; #pragma unroll
;         for (int t = 0; t < 2; ++t) { const LAS bf16_t* kp = KC + (cc * 32 + ki + 4 * t) * 72 + 8 * g; kc[t][0] = *(const LAS bf16x8*)kp; kc[t][1] = *(const LAS bf16x8*)(kp + 32); }
; #pragma unroll
;         for (int d = 0; d < 4; ++d) vc[d] = *(const LAS bf16x8*)(VC + (d * 16 + i) * 264 + cc * 32 + 8 * g);
;         NA_QK(kc, sc);
; #pragma unroll
;         for (int t = 0; t < 2; ++t)
; #pragma unroll
;             for (int e = 0; e < 4; ++e) { const float p = __builtin_amdgcn_exp2f(fminf(sc[t][e], NA_CLAMP)); sc[t][e] = p; lsum += p; }
;         NA_PV(sc, vc);
;     }
;     if (WIN) {
;         const int c = strip * 16 + i; int kc0 = c - 8; kc0 = kc0 < 0 ? 0 : (kc0 > 48 ? 48 : kc0);
;         int dcl[2][4]; bool okm[2][4];
; #pragma unroll
;         for (int t = 0; t < 2; ++t)
; #pragma unroll
;             for (int e = 0; e < 4; ++e) { const int kc = u0 + 8 * g + 4 * t + e; okm[t][e] = (kc >= kc0) && (kc < kc0 + 16); int dc = kc - c + 15; dcl[t][e] = okm[t][e] ? (dc < 0 ? 0 : (dc > 30 ? 30 : dc)) : 31; }
;     ...
;         NA_WCHUNK(vA, 0); NA_SB(); NA_WLOAD(vA, 3); NA_SB();
	v_mfma_f32_16x16x32_bf16 v[84:87], v[44:47], v[12:15], 0
	v_exp_f32_e32 v39, v39
	v_add_f32_e32 v198, v198, v32
	v_add_f32_e32 v199, v199, v36
	v_mfma_f32_16x16x32_bf16 v[90:93], v[52:55], v[12:15], 0
	v_add_f32_e32 v198, v198, v33
	v_add_f32_e32 v199, v199, v37
	v_add_f32_e32 v198, v198, v34
	v_mfma_f32_16x16x32_bf16 v[84:87], v[48:51], v[8:11], v[84:87]
	v_add_f32_e32 v199, v199, v38
	v_add_f32_e32 v198, v198, v35
	v_add_f32_e32 v199, v199, v39
	v_mfma_f32_16x16x32_bf16 v[90:93], v[56:59], v[8:11], v[90:93]
	v_cvt_pk_bf16_f32 v40, v32, v33
	v_cvt_pk_bf16_f32 v41, v34, v35
	v_cvt_pk_bf16_f32 v42, v36, v37
	v_cvt_pk_bf16_f32 v43, v38, v39
	s_mul_i32 s0, s19, 0x2400
	v_add_u32_e32 v203, s0, v202
	s_add_i32 s19, s19, 1
	s_cmp_eq_u32 s19, 9
	s_cselect_b32 s19, 0, s19
	ds_read_b128 v[44:47], v203 offset:0
	ds_read_b128 v[48:51], v203 offset:64
	ds_read_b128 v[52:55], v203 offset:576
	ds_read_b128 v[56:59], v203 offset:640
	ds_read_b32 v76, v216 offset:0
	ds_read_b32 v77, v217 offset:0
	ds_read_b32 v78, v218 offset:0
	ds_read_b32 v79, v219 offset:0
	ds_read_b32 v80, v220 offset:0
	ds_read_b32 v81, v221 offset:0
	ds_read_b32 v82, v222 offset:0
	ds_read_b32 v83, v223 offset:0
	v_min_f32_e32 v84, s18, v84
	v_min_f32_e32 v85, s18, v85
	v_min_f32_e32 v86, s18, v86
	s_waitcnt lgkmcnt(12)
	v_mfma_f32_16x16x32_bf16 v[16:19], v[60:63], v[40:43], v[16:19]
	v_min_f32_e32 v87, s18, v87
	v_min_f32_e32 v90, s18, v90
	v_min_f32_e32 v91, s18, v91
	v_mfma_f32_16x16x32_bf16 v[20:23], v[64:67], v[40:43], v[20:23]
	v_min_f32_e32 v92, s18, v92
	v_min_f32_e32 v93, s18, v93
	v_exp_f32_e32 v84, v84
	v_mfma_f32_16x16x32_bf16 v[24:27], v[68:71], v[40:43], v[24:27]
	v_exp_f32_e32 v85, v85
	v_exp_f32_e32 v86, v86
	v_exp_f32_e32 v87, v87
	v_mfma_f32_16x16x32_bf16 v[28:31], v[72:75], v[40:43], v[28:31]
	ds_read_b128 v[60:63], v201 offset:448
	ds_read_b128 v[64:67], v201 offset:8896
	ds_read_b128 v[68:71], v201 offset:17344
	ds_read_b128 v[72:75], v201 offset:25792
	v_exp_f32_e32 v90, v90
	v_exp_f32_e32 v91, v91
	v_exp_f32_e32 v92, v92
	s_waitcnt lgkmcnt(12)
	v_mfma_f32_16x16x32_bf16 v[32:35], v[44:47], v[12:15], 0
	v_exp_f32_e32 v93, v93
	v_add_f32_e32 v198, v198, v84
	v_add_f32_e32 v199, v199, v90
	v_mfma_f32_16x16x32_bf16 v[36:39], v[52:55], v[12:15], 0
	v_add_f32_e32 v198, v198, v85
	v_add_f32_e32 v199, v199, v91
	v_add_f32_e32 v198, v198, v86
	v_mfma_f32_16x16x32_bf16 v[32:35], v[48:51], v[8:11], v[32:35]
	v_add_f32_e32 v199, v199, v92
	v_add_f32_e32 v198, v198, v87
	v_add_f32_e32 v199, v199, v93
	v_mfma_f32_16x16x32_bf16 v[36:39], v[56:59], v[8:11], v[36:39]
	v_cvt_pk_bf16_f32 v142, v84, v85
	v_cvt_pk_bf16_f32 v143, v86, v87
	v_cvt_pk_bf16_f32 v144, v90, v91
	v_cvt_pk_bf16_f32 v145, v92, v93
	s_mul_i32 s0, s19, 0x2400
	v_add_u32_e32 v203, s0, v202
	s_add_i32 s19, s19, 1
	s_cmp_eq_u32 s19, 9
	s_cselect_b32 s19, 0, s19
	ds_read_b128 v[44:47], v203 offset:0
	ds_read_b128 v[48:51], v203 offset:64
	ds_read_b128 v[52:55], v203 offset:576
	ds_read_b128 v[56:59], v203 offset:640
	ds_read_b32 v188, v216 offset:128
	ds_read_b32 v189, v217 offset:128
	ds_read_b32 v190, v218 offset:128
	ds_read_b32 v191, v219 offset:128
	ds_read_b32 v194, v220 offset:128
	ds_read_b32 v195, v221 offset:128
	ds_read_b32 v196, v222 offset:128
	ds_read_b32 v197, v223 offset:128
	s_waitcnt lgkmcnt(15)
	v_add_f32_e32 v32, v32, v76
	v_add_f32_e32 v33, v33, v77
	v_add_f32_e32 v34, v34, v78
	s_waitcnt lgkmcnt(12)
	v_mfma_f32_16x16x32_bf16 v[16:19], v[60:63], v[142:145], v[16:19]
	v_add_f32_e32 v35, v35, v79
	v_add_f32_e32 v36, v36, v80
	v_add_f32_e32 v37, v37, v81
	v_mfma_f32_16x16x32_bf16 v[20:23], v[64:67], v[142:145], v[20:23]
	v_add_f32_e32 v38, v38, v82
	v_add_f32_e32 v39, v39, v83
	v_min_f32_e32 v32, s18, v32
	v_mfma_f32_16x16x32_bf16 v[24:27], v[68:71], v[142:145], v[24:27]
	v_min_f32_e32 v33, s18, v33
	v_min_f32_e32 v34, s18, v34
	v_min_f32_e32 v35, s18, v35
	v_mfma_f32_16x16x32_bf16 v[28:31], v[72:75], v[142:145], v[28:31]
	v_min_f32_e32 v36, s18, v36
	v_min_f32_e32 v37, s18, v37
	v_min_f32_e32 v38, s18, v38
	s_waitcnt lgkmcnt(8)
	v_mfma_f32_16x16x32_bf16 v[84:87], v[44:47], v[12:15], 0
	v_min_f32_e32 v39, s18, v39
	v_exp_f32_e32 v32, v32
	v_exp_f32_e32 v33, v33
	v_mfma_f32_16x16x32_bf16 v[90:93], v[52:55], v[12:15], 0
	v_exp_f32_e32 v34, v34
	v_exp_f32_e32 v35, v35
	v_exp_f32_e32 v36, v36
	v_mfma_f32_16x16x32_bf16 v[84:87], v[48:51], v[8:11], v[84:87]
	v_exp_f32_e32 v37, v37
	v_exp_f32_e32 v38, v38
	v_exp_f32_e32 v39, v39
	v_mfma_f32_16x16x32_bf16 v[90:93], v[56:59], v[8:11], v[90:93]
	v_add_f32_e32 v198, v198, v32
	v_add_f32_e32 v199, v199, v36
	v_add_f32_e32 v198, v198, v33
	v_add_f32_e32 v199, v199, v37
	v_add_f32_e32 v198, v198, v34
	v_add_f32_e32 v199, v199, v38
	v_add_f32_e32 v198, v198, v35
	v_add_f32_e32 v199, v199, v39
	v_cvt_pk_bf16_f32 v40, v32, v33
	v_cvt_pk_bf16_f32 v41, v34, v35
	v_cvt_pk_bf16_f32 v42, v36, v37
	v_cvt_pk_bf16_f32 v43, v38, v39
	s_mul_i32 s0, s19, 0x2400
	v_add_u32_e32 v203, s0, v202
	s_add_i32 s19, s19, 1
	s_cmp_eq_u32 s19, 9
	s_cselect_b32 s19, 0, s19
	ds_read_b128 v[44:47], v203 offset:0
	ds_read_b128 v[48:51], v203 offset:64
	ds_read_b128 v[52:55], v203 offset:576
	ds_read_b128 v[56:59], v203 offset:640
	ds_read_b32 v76, v216 offset:256
	ds_read_b32 v77, v217 offset:256
	ds_read_b32 v78, v218 offset:256
	ds_read_b32 v79, v219 offset:256
	ds_read_b32 v80, v220 offset:256
	ds_read_b32 v81, v221 offset:256
	ds_read_b32 v82, v222 offset:256
	ds_read_b32 v83, v223 offset:256
	s_waitcnt lgkmcnt(12)
	v_add_f32_e32 v84, v84, v188
	v_add_f32_e32 v85, v85, v189
	v_add_f32_e32 v86, v86, v190
	s_waitcnt vmcnt(12)
; #define NA_SB() __builtin_amdgcn_sched_barrier(0)
; #define NA_WLOAD(vb_, cw) do { _Pragma("unroll") for (int d = 0; d < 4; ++d) vb_[d] = gld16o(vbase + ((size_t)(d * 16) * SPB + (cw) * 64) * 2, vlo); } while (0)
; template <bool WIN>
; __device__ __forceinline__ void na_unit(Frame& F, int b, int h, int r, int strip) {
;     ...
;         NA_WCHUNK(vA, 0); NA_SB(); NA_WLOAD(vA, 3); NA_SB();
;         NA_WCHUNK(vB, 1); NA_SB(); NA_WLOAD(vB, 4); NA_SB();
;         NA_WCHUNK(vC, 2); NA_SB(); NA_WLOAD(vC, 5); NA_SB();
;         NA_WCHUNK(vA, 3); NA_SB(); NA_WLOAD(vA, 6); NA_SB();
;         NA_WCHUNK(vB, 4); NA_SB(); NA_WLOAD(vB, 7); NA_SB();
	v_mfma_f32_16x16x32_bf16 v[16:19], v[104:107], v[40:43], v[16:19]
	v_add_f32_e32 v87, v87, v191
	v_add_f32_e32 v90, v90, v194
	v_add_f32_e32 v91, v91, v195
	v_mfma_f32_16x16x32_bf16 v[20:23], v[108:111], v[40:43], v[20:23]
	v_add_f32_e32 v92, v92, v196
	v_add_f32_e32 v93, v93, v197
	v_min_f32_e32 v84, s18, v84
	v_mfma_f32_16x16x32_bf16 v[24:27], v[112:115], v[40:43], v[24:27]
	v_min_f32_e32 v85, s18, v85
	v_min_f32_e32 v86, s18, v86
	v_min_f32_e32 v87, s18, v87
	v_mfma_f32_16x16x32_bf16 v[28:31], v[116:119], v[40:43], v[28:31]
	global_load_dwordx4 v[104:107], v204, s[20:21] offset:512
	global_load_dwordx4 v[108:111], v205, s[20:21] offset:512
	global_load_dwordx4 v[112:115], v206, s[20:21] offset:512
	global_load_dwordx4 v[116:119], v207, s[20:21] offset:512
	v_min_f32_e32 v90, s18, v90
	v_min_f32_e32 v91, s18, v91
	v_min_f32_e32 v92, s18, v92
	s_waitcnt lgkmcnt(8)
	v_mfma_f32_16x16x32_bf16 v[32:35], v[44:47], v[12:15], 0
	v_min_f32_e32 v93, s18, v93
	v_exp_f32_e32 v84, v84
	v_exp_f32_e32 v85, v85
	v_mfma_f32_16x16x32_bf16 v[36:39], v[52:55], v[12:15], 0
	v_exp_f32_e32 v86, v86
	v_exp_f32_e32 v87, v87
	v_exp_f32_e32 v90, v90
	v_mfma_f32_16x16x32_bf16 v[32:35], v[48:51], v[8:11], v[32:35]
	v_exp_f32_e32 v91, v91
	v_exp_f32_e32 v92, v92
	v_exp_f32_e32 v93, v93
	v_mfma_f32_16x16x32_bf16 v[36:39], v[56:59], v[8:11], v[36:39]
	v_add_f32_e32 v198, v198, v84
	v_add_f32_e32 v199, v199, v90
	v_add_f32_e32 v198, v198, v85
	v_add_f32_e32 v199, v199, v91
	v_add_f32_e32 v198, v198, v86
	v_add_f32_e32 v199, v199, v92
	v_add_f32_e32 v198, v198, v87
	v_add_f32_e32 v199, v199, v93
	v_cvt_pk_bf16_f32 v142, v84, v85
	v_cvt_pk_bf16_f32 v143, v86, v87
	v_cvt_pk_bf16_f32 v144, v90, v91
	v_cvt_pk_bf16_f32 v145, v92, v93
	s_mul_i32 s0, s19, 0x2400
	v_add_u32_e32 v203, s0, v202
	s_add_i32 s19, s19, 1
	s_cmp_eq_u32 s19, 9
	s_cselect_b32 s19, 0, s19
	ds_read_b128 v[44:47], v203 offset:0
	ds_read_b128 v[48:51], v203 offset:64
	ds_read_b128 v[52:55], v203 offset:576
	ds_read_b128 v[56:59], v203 offset:640
	ds_read_b32 v188, v216 offset:384
	ds_read_b32 v189, v217 offset:384
	ds_read_b32 v190, v218 offset:384
	ds_read_b32 v191, v219 offset:384
	ds_read_b32 v194, v220 offset:384
	ds_read_b32 v195, v221 offset:384
	ds_read_b32 v196, v222 offset:384
	ds_read_b32 v197, v223 offset:384
	s_waitcnt lgkmcnt(12)
	v_add_f32_e32 v32, v32, v76
	v_add_f32_e32 v33, v33, v77
	v_add_f32_e32 v34, v34, v78
	s_waitcnt vmcnt(12)
	v_mfma_f32_16x16x32_bf16 v[16:19], v[120:123], v[142:145], v[16:19]
	v_add_f32_e32 v35, v35, v79
	v_add_f32_e32 v36, v36, v80
	v_add_f32_e32 v37, v37, v81
	v_mfma_f32_16x16x32_bf16 v[20:23], v[124:127], v[142:145], v[20:23]
	v_add_f32_e32 v38, v38, v82
	v_add_f32_e32 v39, v39, v83
	v_min_f32_e32 v32, s18, v32
	v_mfma_f32_16x16x32_bf16 v[24:27], v[128:131], v[142:145], v[24:27]
	v_min_f32_e32 v33, s18, v33
	v_min_f32_e32 v34, s18, v34
	v_min_f32_e32 v35, s18, v35
	v_mfma_f32_16x16x32_bf16 v[28:31], v[132:135], v[142:145], v[28:31]
	global_load_dwordx4 v[120:123], v204, s[20:21] offset:640
	global_load_dwordx4 v[124:127], v205, s[20:21] offset:640
	global_load_dwordx4 v[128:131], v206, s[20:21] offset:640
	global_load_dwordx4 v[132:135], v207, s[20:21] offset:640
	v_min_f32_e32 v36, s18, v36
	v_min_f32_e32 v37, s18, v37
	v_min_f32_e32 v38, s18, v38
	s_waitcnt lgkmcnt(8)
	v_mfma_f32_16x16x32_bf16 v[84:87], v[44:47], v[12:15], 0
	v_min_f32_e32 v39, s18, v39
	v_exp_f32_e32 v32, v32
	v_exp_f32_e32 v33, v33
	v_mfma_f32_16x16x32_bf16 v[90:93], v[52:55], v[12:15], 0
	v_exp_f32_e32 v34, v34
	v_exp_f32_e32 v35, v35
	v_exp_f32_e32 v36, v36
	v_mfma_f32_16x16x32_bf16 v[84:87], v[48:51], v[8:11], v[84:87]
	v_exp_f32_e32 v37, v37
	v_exp_f32_e32 v38, v38
	v_exp_f32_e32 v39, v39
	v_mfma_f32_16x16x32_bf16 v[90:93], v[56:59], v[8:11], v[90:93]
	v_add_f32_e32 v198, v198, v32
	v_add_f32_e32 v199, v199, v36
	v_add_f32_e32 v198, v198, v33
	v_add_f32_e32 v199, v199, v37
	v_add_f32_e32 v198, v198, v34
	v_add_f32_e32 v199, v199, v38
	v_add_f32_e32 v198, v198, v35
	v_add_f32_e32 v199, v199, v39
	v_cvt_pk_bf16_f32 v40, v32, v33
	v_cvt_pk_bf16_f32 v41, v34, v35
	v_cvt_pk_bf16_f32 v42, v36, v37
	v_cvt_pk_bf16_f32 v43, v38, v39
	s_mul_i32 s0, s19, 0x2400
	v_add_u32_e32 v203, s0, v202
	s_add_i32 s19, s19, 1
	s_cmp_eq_u32 s19, 9
	s_cselect_b32 s19, 0, s19
	ds_read_b128 v[44:47], v203 offset:0
	ds_read_b128 v[48:51], v203 offset:64
	ds_read_b128 v[52:55], v203 offset:576
	ds_read_b128 v[56:59], v203 offset:640
	ds_read_b32 v76, v216 offset:512
	ds_read_b32 v77, v217 offset:512
	ds_read_b32 v78, v218 offset:512
	ds_read_b32 v79, v219 offset:512
	ds_read_b32 v80, v220 offset:512
	ds_read_b32 v81, v221 offset:512
	ds_read_b32 v82, v222 offset:512
	ds_read_b32 v83, v223 offset:512
	s_waitcnt lgkmcnt(12)
	v_add_f32_e32 v84, v84, v188
	v_add_f32_e32 v85, v85, v189
	v_add_f32_e32 v86, v86, v190
	s_waitcnt vmcnt(12)
	v_mfma_f32_16x16x32_bf16 v[16:19], v[156:159], v[40:43], v[16:19]
	v_add_f32_e32 v87, v87, v191
	v_add_f32_e32 v90, v90, v194
	v_add_f32_e32 v91, v91, v195
	v_mfma_f32_16x16x32_bf16 v[20:23], v[160:163], v[40:43], v[20:23]
	v_add_f32_e32 v92, v92, v196
	v_add_f32_e32 v93, v93, v197
	v_min_f32_e32 v84, s18, v84
	v_mfma_f32_16x16x32_bf16 v[24:27], v[164:167], v[40:43], v[24:27]
	v_min_f32_e32 v85, s18, v85
	v_min_f32_e32 v86, s18, v86
	v_min_f32_e32 v87, s18, v87
	v_mfma_f32_16x16x32_bf16 v[28:31], v[168:171], v[40:43], v[28:31]
	global_load_dwordx4 v[156:159], v204, s[20:21] offset:768
	global_load_dwordx4 v[160:163], v205, s[20:21] offset:768
	global_load_dwordx4 v[164:167], v206, s[20:21] offset:768
	global_load_dwordx4 v[168:171], v207, s[20:21] offset:768
	v_min_f32_e32 v90, s18, v90
	v_min_f32_e32 v91, s18, v91
	v_min_f32_e32 v92, s18, v92
	s_waitcnt lgkmcnt(8)
; #define NA_SB() __builtin_amdgcn_sched_barrier(0)
; #define NA_WLOAD(vb_, cw) do { _Pragma("unroll") for (int d = 0; d < 4; ++d) vb_[d] = gld16o(vbase + ((size_t)(d * 16) * SPB + (cw) * 64) * 2, vlo); } while (0)
; template <bool WIN>
; __device__ __forceinline__ void na_unit(Frame& F, int b, int h, int r, int strip) {
;     ...
;         NA_WCHUNK(vA, 0); NA_SB(); NA_WLOAD(vA, 3); NA_SB();
;         NA_WCHUNK(vB, 1); NA_SB(); NA_WLOAD(vB, 4); NA_SB();
;         NA_WCHUNK(vC, 2); NA_SB(); NA_WLOAD(vC, 5); NA_SB();
;         NA_WCHUNK(vA, 3); NA_SB(); NA_WLOAD(vA, 6); NA_SB();
;         NA_WCHUNK(vB, 4); NA_SB(); NA_WLOAD(vB, 7); NA_SB();
	v_mfma_f32_16x16x32_bf16 v[32:35], v[44:47], v[12:15], 0
	v_min_f32_e32 v93, s18, v93
	v_exp_f32_e32 v84, v84
	v_exp_f32_e32 v85, v85
	v_mfma_f32_16x16x32_bf16 v[36:39], v[52:55], v[12:15], 0
	v_exp_f32_e32 v86, v86
	v_exp_f32_e32 v87, v87
	v_exp_f32_e32 v90, v90
	v_mfma_f32_16x16x32_bf16 v[32:35], v[48:51], v[8:11], v[32:35]
	v_exp_f32_e32 v91, v91
	v_exp_f32_e32 v92, v92
	v_exp_f32_e32 v93, v93
	v_mfma_f32_16x16x32_bf16 v[36:39], v[56:59], v[8:11], v[36:39]
	v_add_f32_e32 v198, v198, v84
	v_add_f32_e32 v199, v199, v90
	v_add_f32_e32 v198, v198, v85
	v_add_f32_e32 v199, v199, v91
	v_add_f32_e32 v198, v198, v86
	v_add_f32_e32 v199, v199, v92
	v_add_f32_e32 v198, v198, v87
	v_add_f32_e32 v199, v199, v93
	v_cvt_pk_bf16_f32 v142, v84, v85
	v_cvt_pk_bf16_f32 v143, v86, v87
	v_cvt_pk_bf16_f32 v144, v90, v91
	v_cvt_pk_bf16_f32 v145, v92, v93
	s_mul_i32 s0, s19, 0x2400
	v_add_u32_e32 v203, s0, v202
	s_add_i32 s19, s19, 1
	s_cmp_eq_u32 s19, 9
	s_cselect_b32 s19, 0, s19
	ds_read_b128 v[44:47], v203 offset:0
	ds_read_b128 v[48:51], v203 offset:64
	ds_read_b128 v[52:55], v203 offset:576
	ds_read_b128 v[56:59], v203 offset:640
	ds_read_b32 v188, v216 offset:640
	ds_read_b32 v189, v217 offset:640
	ds_read_b32 v190, v218 offset:640
	ds_read_b32 v191, v219 offset:640
	ds_read_b32 v194, v220 offset:640
	ds_read_b32 v195, v221 offset:640
	ds_read_b32 v196, v222 offset:640
	ds_read_b32 v197, v223 offset:640
	s_waitcnt lgkmcnt(12)
	v_add_f32_e32 v32, v32, v76
	v_add_f32_e32 v33, v33, v77
	v_add_f32_e32 v34, v34, v78
	s_waitcnt vmcnt(12)
	v_mfma_f32_16x16x32_bf16 v[16:19], v[172:175], v[142:145], v[16:19]
	v_add_f32_e32 v35, v35, v79
	v_add_f32_e32 v36, v36, v80
	v_add_f32_e32 v37, v37, v81
	v_mfma_f32_16x16x32_bf16 v[20:23], v[176:179], v[142:145], v[20:23]
	v_add_f32_e32 v38, v38, v82
	v_add_f32_e32 v39, v39, v83
	v_min_f32_e32 v32, s18, v32
	v_mfma_f32_16x16x32_bf16 v[24:27], v[180:183], v[142:145], v[24:27]
	v_min_f32_e32 v33, s18, v33
	v_min_f32_e32 v34, s18, v34
	v_min_f32_e32 v35, s18, v35
	v_mfma_f32_16x16x32_bf16 v[28:31], v[184:187], v[142:145], v[28:31]
	global_load_dwordx4 v[172:175], v204, s[20:21] offset:896
	global_load_dwordx4 v[176:179], v205, s[20:21] offset:896
	global_load_dwordx4 v[180:183], v206, s[20:21] offset:896
	global_load_dwordx4 v[184:187], v207, s[20:21] offset:896
	v_min_f32_e32 v36, s18, v36
	v_min_f32_e32 v37, s18, v37
	v_min_f32_e32 v38, s18, v38
	s_waitcnt lgkmcnt(8)
	v_mfma_f32_16x16x32_bf16 v[84:87], v[44:47], v[12:15], 0
	v_min_f32_e32 v39, s18, v39
	v_exp_f32_e32 v32, v32
	v_exp_f32_e32 v33, v33
	v_mfma_f32_16x16x32_bf16 v[90:93], v[52:55], v[12:15], 0
	v_exp_f32_e32 v34, v34
	v_exp_f32_e32 v35, v35
	v_exp_f32_e32 v36, v36
	v_mfma_f32_16x16x32_bf16 v[84:87], v[48:51], v[8:11], v[84:87]
	v_exp_f32_e32 v37, v37
	v_exp_f32_e32 v38, v38
	v_exp_f32_e32 v39, v39
	v_mfma_f32_16x16x32_bf16 v[90:93], v[56:59], v[8:11], v[90:93]
	v_add_f32_e32 v198, v198, v32
	v_add_f32_e32 v199, v199, v36
	v_add_f32_e32 v198, v198, v33
	v_add_f32_e32 v199, v199, v37
	v_add_f32_e32 v198, v198, v34
	v_add_f32_e32 v199, v199, v38
	v_add_f32_e32 v198, v198, v35
	v_add_f32_e32 v199, v199, v39
	v_cvt_pk_bf16_f32 v40, v32, v33
	v_cvt_pk_bf16_f32 v41, v34, v35
	v_cvt_pk_bf16_f32 v42, v36, v37
	v_cvt_pk_bf16_f32 v43, v38, v39
	s_mul_i32 s0, s19, 0x2400
	v_add_u32_e32 v203, s0, v202
	s_add_i32 s19, s19, 1
	s_cmp_eq_u32 s19, 9
	s_cselect_b32 s19, 0, s19
	ds_read_b128 v[44:47], v203 offset:0
	ds_read_b128 v[48:51], v203 offset:64
	ds_read_b128 v[52:55], v203 offset:576
	ds_read_b128 v[56:59], v203 offset:640
	ds_read_b32 v76, v216 offset:768
	ds_read_b32 v77, v217 offset:768
	ds_read_b32 v78, v218 offset:768
	ds_read_b32 v79, v219 offset:768
	ds_read_b32 v80, v220 offset:768
	ds_read_b32 v81, v221 offset:768
	ds_read_b32 v82, v222 offset:768
	ds_read_b32 v83, v223 offset:768
	s_waitcnt lgkmcnt(12)
	v_add_f32_e32 v84, v84, v188
	v_add_f32_e32 v85, v85, v189
	v_add_f32_e32 v86, v86, v190
	s_waitcnt vmcnt(12)
	v_mfma_f32_16x16x32_bf16 v[16:19], v[104:107], v[40:43], v[16:19]
	v_add_f32_e32 v87, v87, v191
	v_add_f32_e32 v90, v90, v194
	v_add_f32_e32 v91, v91, v195
	v_mfma_f32_16x16x32_bf16 v[20:23], v[108:111], v[40:43], v[20:23]
	v_add_f32_e32 v92, v92, v196
	v_add_f32_e32 v93, v93, v197
	v_min_f32_e32 v84, s18, v84
	v_mfma_f32_16x16x32_bf16 v[24:27], v[112:115], v[40:43], v[24:27]
	v_min_f32_e32 v85, s18, v85
	v_min_f32_e32 v86, s18, v86
	v_min_f32_e32 v87, s18, v87
	v_mfma_f32_16x16x32_bf16 v[28:31], v[116:119], v[40:43], v[28:31]
	v_min_f32_e32 v90, s18, v90
	v_min_f32_e32 v91, s18, v91
	v_min_f32_e32 v92, s18, v92
	s_waitcnt lgkmcnt(8)
	v_mfma_f32_16x16x32_bf16 v[32:35], v[44:47], v[12:15], 0
	v_min_f32_e32 v93, s18, v93
	v_exp_f32_e32 v84, v84
	v_exp_f32_e32 v85, v85
	v_mfma_f32_16x16x32_bf16 v[36:39], v[52:55], v[12:15], 0
	v_exp_f32_e32 v86, v86
	v_exp_f32_e32 v87, v87
	v_exp_f32_e32 v90, v90
	v_mfma_f32_16x16x32_bf16 v[32:35], v[48:51], v[8:11], v[32:35]
	v_exp_f32_e32 v91, v91
	v_exp_f32_e32 v92, v92
	v_exp_f32_e32 v93, v93
	v_mfma_f32_16x16x32_bf16 v[36:39], v[56:59], v[8:11], v[36:39]
	v_add_f32_e32 v198, v198, v84
	v_add_f32_e32 v199, v199, v90
	v_add_f32_e32 v198, v198, v85
	v_add_f32_e32 v199, v199, v91
	v_add_f32_e32 v198, v198, v86
	v_add_f32_e32 v199, v199, v92
	v_add_f32_e32 v198, v198, v87
	v_add_f32_e32 v199, v199, v93
	v_cvt_pk_bf16_f32 v142, v84, v85
	v_cvt_pk_bf16_f32 v143, v86, v87
	v_cvt_pk_bf16_f32 v144, v90, v91
	v_cvt_pk_bf16_f32 v145, v92, v93
	s_mul_i32 s0, s19, 0x2400
	v_add_u32_e32 v203, s0, v202
	s_add_i32 s19, s19, 1
	s_cmp_eq_u32 s19, 9
	s_cselect_b32 s19, 0, s19
	ds_read_b128 v[44:47], v203 offset:0
	ds_read_b128 v[48:51], v203 offset:64
	ds_read_b128 v[52:55], v203 offset:576
	ds_read_b128 v[56:59], v203 offset:640
	ds_read_b32 v188, v216 offset:896
	ds_read_b32 v189, v217 offset:896
	ds_read_b32 v190, v218 offset:896
	ds_read_b32 v191, v219 offset:896
	ds_read_b32 v194, v220 offset:896
	ds_read_b32 v195, v221 offset:896
	ds_read_b32 v196, v222 offset:896
	ds_read_b32 v197, v223 offset:896
	s_waitcnt lgkmcnt(12)
; #define GAS __attribute__((address_space(1)))
; __device__ __forceinline__ unsigned pk2(float lo, float hi) { const f32x2 v = {lo, hi}; const bf16v2 b = __builtin_convertvector(v, bf16v2); return __builtin_bit_cast(unsigned, b); }
; __device__ __forceinline__ float shx(float v, int o, int lane) { return __builtin_bit_cast(float, __builtin_amdgcn_ds_bpermute((lane ^ o) << 2, __builtin_bit_cast(int, v))); }
; __device__ __forceinline__ const char* uni_ptr(const char* p) { const unsigned long long v = (unsigned long long)p; const unsigned lo = __builtin_amdgcn_readfirstlane((unsigned)v), hi = __builtin_amdgcn_readfirstlane((unsigned)(v >> 32)); return (const char*)(((unsigned long long)hi << 32) | lo); }
; #define NA_SB() __builtin_amdgcn_sched_barrier(0)
; #define NA_WLOAD(vb_, cw) do { _Pragma("unroll") for (int d = 0; d < 4; ++d) vb_[d] = gld16o(vbase + ((size_t)(d * 16) * SPB + (cw) * 64) * 2, vlo); } while (0)
; template <bool WIN>
; __device__ __forceinline__ void na_unit(Frame& F, int b, int h, int r, int strip) {
;     ...
;         NA_WCHUNK(vC, 2); NA_SB(); NA_WLOAD(vC, 5); NA_SB();
;         NA_WCHUNK(vA, 3); NA_SB(); NA_WLOAD(vA, 6); NA_SB();
;         NA_WCHUNK(vB, 4); NA_SB(); NA_WLOAD(vB, 7); NA_SB();
;         NA_WCHUNK(vC, 5); NA_SB();
;         NA_WCHUNK(vA, 6); NA_SB();
;         NA_WCHUNK(vB, 7); NA_SB();
;     ...
;     }
;     lsum += shx(lsum, 16, ln_); lsum += shx(lsum, 32, ln_);
;     const float inv = 1.0f / lsum;
;     char* op = (char*)uni_ptr((const char*)((bf16_t*)(F.ws + WS_MIX) + (size_t)qrow0 * DM + h * 64)); const unsigned olo = (unsigned)((i * DM + 4 * g) * 2);
; #pragma unroll
;     for (int d = 0; d < 4; ++d) { u32x2 w; w.x = pk2(o[d][0] * inv, o[d][1] * inv); w.y = pk2(o[d][2] * inv, o[d][3] * inv); *(GAS u32x2*)(op + d * 32 + (size_t)olo) = w; }
	v_add_f32_e32 v32, v32, v76
	v_add_f32_e32 v33, v33, v77
	v_add_f32_e32 v34, v34, v78
	s_waitcnt vmcnt(8)
	v_mfma_f32_16x16x32_bf16 v[16:19], v[120:123], v[142:145], v[16:19]
	v_add_f32_e32 v35, v35, v79
	v_add_f32_e32 v36, v36, v80
	v_add_f32_e32 v37, v37, v81
	v_mfma_f32_16x16x32_bf16 v[20:23], v[124:127], v[142:145], v[20:23]
	v_add_f32_e32 v38, v38, v82
	v_add_f32_e32 v39, v39, v83
	v_min_f32_e32 v32, s18, v32
	v_mfma_f32_16x16x32_bf16 v[24:27], v[128:131], v[142:145], v[24:27]
	v_min_f32_e32 v33, s18, v33
	v_min_f32_e32 v34, s18, v34
	v_min_f32_e32 v35, s18, v35
	v_mfma_f32_16x16x32_bf16 v[28:31], v[132:135], v[142:145], v[28:31]
	v_min_f32_e32 v36, s18, v36
	v_min_f32_e32 v37, s18, v37
	v_min_f32_e32 v38, s18, v38
	s_waitcnt lgkmcnt(8)
	v_mfma_f32_16x16x32_bf16 v[84:87], v[44:47], v[12:15], 0
	v_min_f32_e32 v39, s18, v39
	v_exp_f32_e32 v32, v32
	v_exp_f32_e32 v33, v33
	v_mfma_f32_16x16x32_bf16 v[90:93], v[52:55], v[12:15], 0
	v_exp_f32_e32 v34, v34
	v_exp_f32_e32 v35, v35
	v_exp_f32_e32 v36, v36
	v_mfma_f32_16x16x32_bf16 v[84:87], v[48:51], v[8:11], v[84:87]
	v_exp_f32_e32 v37, v37
	v_exp_f32_e32 v38, v38
	v_exp_f32_e32 v39, v39
	v_mfma_f32_16x16x32_bf16 v[90:93], v[56:59], v[8:11], v[90:93]
	v_add_f32_e32 v198, v198, v32
	v_add_f32_e32 v199, v199, v36
	v_add_f32_e32 v198, v198, v33
	v_add_f32_e32 v199, v199, v37
	v_add_f32_e32 v198, v198, v34
	v_add_f32_e32 v199, v199, v38
	v_add_f32_e32 v198, v198, v35
	v_add_f32_e32 v199, v199, v39
	v_cvt_pk_bf16_f32 v40, v32, v33
	v_cvt_pk_bf16_f32 v41, v34, v35
	v_cvt_pk_bf16_f32 v42, v36, v37
	v_cvt_pk_bf16_f32 v43, v38, v39
	s_waitcnt lgkmcnt(0)
	v_add_f32_e32 v84, v84, v188
	v_add_f32_e32 v85, v85, v189
	v_add_f32_e32 v86, v86, v190
	s_waitcnt vmcnt(4)
	v_mfma_f32_16x16x32_bf16 v[16:19], v[156:159], v[40:43], v[16:19]
	v_add_f32_e32 v87, v87, v191
	v_add_f32_e32 v90, v90, v194
	v_add_f32_e32 v91, v91, v195
	v_mfma_f32_16x16x32_bf16 v[20:23], v[160:163], v[40:43], v[20:23]
	v_add_f32_e32 v92, v92, v196
	v_add_f32_e32 v93, v93, v197
	v_min_f32_e32 v84, s18, v84
	v_mfma_f32_16x16x32_bf16 v[24:27], v[164:167], v[40:43], v[24:27]
	v_min_f32_e32 v85, s18, v85
	v_min_f32_e32 v86, s18, v86
	v_min_f32_e32 v87, s18, v87
	v_mfma_f32_16x16x32_bf16 v[28:31], v[168:171], v[40:43], v[28:31]
	v_min_f32_e32 v90, s18, v90
	v_min_f32_e32 v91, s18, v91
	v_min_f32_e32 v92, s18, v92
	v_min_f32_e32 v93, s18, v93
	v_exp_f32_e32 v84, v84
	v_exp_f32_e32 v85, v85
	v_exp_f32_e32 v86, v86
	v_exp_f32_e32 v87, v87
	v_exp_f32_e32 v90, v90
	v_exp_f32_e32 v91, v91
	v_exp_f32_e32 v92, v92
	v_exp_f32_e32 v93, v93
	v_add_f32_e32 v198, v198, v84
	v_add_f32_e32 v199, v199, v90
	v_add_f32_e32 v198, v198, v85
	v_add_f32_e32 v199, v199, v91
	v_add_f32_e32 v198, v198, v86
	v_add_f32_e32 v199, v199, v92
	v_add_f32_e32 v198, v198, v87
	v_add_f32_e32 v199, v199, v93
	v_cvt_pk_bf16_f32 v142, v84, v85
	v_cvt_pk_bf16_f32 v143, v86, v87
	v_cvt_pk_bf16_f32 v144, v90, v91
	v_cvt_pk_bf16_f32 v145, v92, v93
	s_waitcnt vmcnt(0)
	s_nop 0
	v_mfma_f32_16x16x32_bf16 v[16:19], v[172:175], v[142:145], v[16:19]
	v_mfma_f32_16x16x32_bf16 v[20:23], v[176:179], v[142:145], v[20:23]
	v_mfma_f32_16x16x32_bf16 v[24:27], v[180:183], v[142:145], v[24:27]
	v_mfma_f32_16x16x32_bf16 v[28:31], v[184:187], v[142:145], v[28:31]
	v_add_f32_e32 v198, v198, v199
	ds_bpermute_b32 v237, v246, v198
	s_waitcnt lgkmcnt(0)
	v_add_f32_e32 v198, v198, v237
	ds_bpermute_b32 v237, v247, v198
	s_waitcnt lgkmcnt(0)
	v_add_f32_e32 v198, v198, v237
	v_rcp_f32_e32 v225, v198
	s_nop 0
	v_fma_f32 v236, -v198, v225, 1.0
	v_fma_f32 v225, v236, v225, v225
	v_mul_f32_e32 v16, v16, v225
	v_mul_f32_e32 v17, v17, v225
	v_mul_f32_e32 v18, v18, v225
	v_mul_f32_e32 v19, v19, v225
	v_mul_f32_e32 v20, v20, v225
	v_mul_f32_e32 v21, v21, v225
	v_mul_f32_e32 v22, v22, v225
	v_mul_f32_e32 v23, v23, v225
	v_mul_f32_e32 v24, v24, v225
	v_mul_f32_e32 v25, v25, v225
	v_mul_f32_e32 v26, v26, v225
	v_mul_f32_e32 v27, v27, v225
	v_mul_f32_e32 v28, v28, v225
	v_mul_f32_e32 v29, v29, v225
	v_mul_f32_e32 v30, v30, v225
	v_mul_f32_e32 v31, v31, v225
	v_cvt_pk_bf16_f32 v16, v16, v17
	v_cvt_pk_bf16_f32 v17, v18, v19
	v_cvt_pk_bf16_f32 v20, v20, v21
	v_cvt_pk_bf16_f32 v21, v22, v23
	v_cvt_pk_bf16_f32 v24, v24, v25
	v_cvt_pk_bf16_f32 v25, v26, v27
	v_cvt_pk_bf16_f32 v28, v28, v29
	v_cvt_pk_bf16_f32 v29, v30, v31
	global_store_dwordx2 v224, v[16:17], s[10:11] offset:0
	global_store_dwordx2 v224, v[20:21], s[10:11] offset:32
	global_store_dwordx2 v224, v[24:25], s[10:11] offset:64
	global_store_dwordx2 v224, v[28:29], s[10:11] offset:96
	s_andn2_b64 vcc, exec, s[50:51]
	s_barrier
	s_cbranch_vccnz .LBB0_495
	s_mul_hi_u32 s0, s84, 0x38e38e39
	s_lshr_b32 s0, s0, 1
	s_mul_i32 s0, s0, 9
	s_sub_i32 s0, s84, s0
	s_mulk_i32 s0, 0x2400
	v_add_u32_e32 v8, s0, v97
	ds_write_b128 v8, v[0:3]
